# baseline (speedup 1.0000x reference)
.Lno_anc:
	s_or_b64 exec, exec, s[8:9]
	v_mov_b32_e32 v7, 0x80
	s_waitcnt vmcnt(0)
	s_sleep 80
	v_cmp_ne_u32_e64 s[4:5], 0, v12
	s_nop 1
	v_cndmask_b32_e64 v8, 0, 1, s[4:5]
	v_cmp_eq_u32_e64 s[4:5], 0, v13
	s_nop 1
	v_cndmask_b32_e64 v9, 2, 0, s[4:5]
	v_cmp_eq_u32_e64 s[4:5], 0, v14
	v_or_b32_e32 v8, v9, v8
	s_nop 0
	v_cndmask_b32_e64 v12, 4, 0, s[4:5]
	v_cmp_eq_u32_e64 s[4:5], 0, v15
	s_nop 1
	v_cndmask_b32_e64 v13, 8, 0, s[4:5]
	v_cmp_eq_u32_e64 s[4:5], 0, v16
	v_or3_b32 v8, v8, v12, v13
	s_nop 0
	v_cndmask_b32_e64 v14, 16, 0, s[4:5]
	v_cmp_eq_u32_e64 s[4:5], 0, v17
	s_nop 1
	v_cndmask_b32_e64 v15, 32, 0, s[4:5]
	v_cmp_eq_u32_e64 s[4:5], 0, v18
	s_nop 1
	v_cndmask_b32_e64 v16, 64, 0, s[4:5]
	v_cmp_eq_u32_e64 s[4:5], 0, v19
	s_nop 1
	v_cndmask_b32_e64 v7, v7, 0, s[4:5]
	v_or_b32_e32 v7, v16, v7
	v_or3_b32 v9, v7, v15, v14
	v_or_b32_e32 v7, v9, v8
	v_bcnt_u32_b32 v8, v8, 0
	v_bcnt_u32_b32 v9, v9, 0
	v_lshl_or_b32 v9, v9, 16, v8
	v_cmp_ne_u32_e64 s[4:5], 0, v7
	s_nop 0
	v_add_u32_dpp v8, v9, v9 row_shr:1 row_mask:0xf bank_mask:0xf bound_ctrl:1
	s_nop 1
	v_add_u32_dpp v8, v8, v8 row_shr:2 row_mask:0xf bank_mask:0xf bound_ctrl:1
	s_nop 1
	v_add_u32_dpp v8, v8, v8 row_shr:4 row_mask:0xf bank_mask:0xf bound_ctrl:1
	s_nop 1
	v_add_u32_dpp v12, v8, v8 row_shr:8 row_mask:0xf bank_mask:0xf bound_ctrl:1
	s_nop 1
	v_add_u32_dpp v12, v12, v12 row_bcast:15 row_mask:0xa bank_mask:0xf
	s_nop 1
	v_add_u32_dpp v12, v12, v12 row_bcast:31 row_mask:0xc bank_mask:0xf
	s_nop 0
	v_readlane_b32 s14, v12, 63
	s_and_b32 s3, s14, 0xffff
	s_and_saveexec_b64 s[10:11], s[4:5]
	s_cbranch_execz .LBB0_5
	v_sub_u32_e32 v12, v12, v9
	v_lshlrev_b32_e32 v8, 10, v1
	v_add_u32_sdwa v9, sext(v12), s3 dst_sel:DWORD dst_unused:UNUSED_PAD src0_sel:WORD_1 src1_sel:DWORD
	v_and_b32_e32 v12, 0xffff, v12
	v_lshlrev_b32_e32 v13, 2, v10
	s_mov_b64 s[12:13], 0
	v_mov_b32_e32 v14, 0x100
